# scan loader: expert-weight tile read with 8 dwordx4 loads per wave (lane = k-group x 4-column group) instead of 32 dword loads; no cross-lane exchange; 12 instead of 36 memory instructions per tile
# speedup vs baseline: 1.0138x; 1.0068x over previous
; __device__ __forceinline__ void p4_scan(const Args& a, const Frame& F) {
;     ...
;             auto prefetch = [&](int ci) {
;                 const int base = chunk_base(ci);
; #pragma unroll
;                 for (int i = 0; i < 8; ++i) { const int p = ht + 256 * i, row = p >> 4, c16 = p & 15; const int tok = base + (dir ? 127 - row : row);
;                     pq[i] = *(const u32x4*)(QKC + (size_t)tok * 1024 + h * 128 + c16 * 8); pk[i] = *(const u32x4*)(QKC + (size_t)tok * 1024 + 512 + h * 128 + c16 * 8); }
;     ...
;             auto conv_load = [&](int it) {
;                 const float* cW; int cN, cn;
;                 if (it < 32768) { const int e = it >> 10, sb = it & 1023; ck0 = (sb >> 6) * 64; cn = (sb & 63) * 32 + (lane & 31); cN = 2048; cW = a.in[IN_W1] + (size_t)e * 1024 * 2048; cD = (bf16*)(a.ws + WS_W1T);
;                     const int up = cn >= 1024, nn = cn & 1023; crow = e * 2048 + (nn >> 7) * 256 + up * 128 + (nn & 127); }
;                 else { const int it2 = it - 32768, e = it2 >> 9, sb = it2 & 511; ck0 = (sb >> 5) * 64; cn = (sb & 31) * 32 + (lane & 31); cN = 1024; cW = a.in[IN_W2] + (size_t)e * 1024 * 1024; cD = (bf16*)(a.ws + WS_W2T); crow = e * 1024 + cn; }
; #pragma unroll
;                 for (int i = 0; i < 32; ++i) cv[i] = cW[(size_t)(ck0 + (lane >> 5) + 2 * i) * cN + cn];
;             };
.LBB0_490:
	v_and_b32_e32 v82, 0x3c0, v9
	v_and_b32_e32 v206, 7, v252
	v_lshlrev_b32_e32 v206, 2, v206
	v_and_b32_e32 v207, 31, v252
	v_sub_u32_e32 v206, v206, v207
	v_and_b32_e32 v207, 0x38, v252
	v_add_u32_e32 v12, v8, v206
	v_add_u32_e32 v14, v82, v207
	v_mul_u32_u24_e32 v14, s54, v14
	v_add_u32_e32 v12, v12, v14
	v_mov_b32_e32 v13, v145
	v_lshl_add_u64 v[12:13], v[12:13], 2, s[56:57]
	global_load_dwordx4 v[174:177], v[12:13], off
	v_lshl_add_u64 v[12:13], s[54:55], 2, v[12:13]
	global_load_dwordx4 v[178:181], v[12:13], off
	v_lshl_add_u64 v[12:13], s[54:55], 2, v[12:13]
	global_load_dwordx4 v[182:185], v[12:13], off
	v_lshl_add_u64 v[12:13], s[54:55], 2, v[12:13]
	global_load_dwordx4 v[138:141], v[12:13], off
	v_lshl_add_u64 v[12:13], s[54:55], 2, v[12:13]
	global_load_dwordx4 v[148:151], v[12:13], off
	v_lshl_add_u64 v[12:13], s[54:55], 2, v[12:13]
	global_load_dwordx4 v[198:201], v[12:13], off
	v_lshl_add_u64 v[12:13], s[54:55], 2, v[12:13]
	global_load_dwordx4 v[202:205], v[12:13], off
	v_lshl_add_u64 v[12:13], s[54:55], 2, v[12:13]
	global_load_dwordx4 v[210:213], v[12:13], off
	s_lshl_b32 s44, s44, 1
	s_add_u32 s54, s20, s44
	s_addc_u32 s55, s21, 0
	s_lshl_b32 s33, s33, 1
	s_add_u32 s54, s54, s33
	s_addc_u32 s55, s55, 0
	v_mov_b32_e32 v87, v145
	v_lshl_add_u64 v[86:87], s[54:55], 0, v[86:87]
	s_add_i32 s54, s34, s35
	v_mov_b64_e32 v[8:9], s[38:39]
	s_add_i32 s33, 0, 0x23430
	v_mad_i64_i32 v[88:89], s[34:35], v88, s95, v[8:9]
	v_mad_i64_i32 v[90:91], s[34:35], v90, s95, v[8:9]
	s_add_i32 s54, s54, 0x10000
	v_add_u32_e32 v12, s33, v11
	s_lshl_b32 s33, s58, 13
	s_xor_b32 s34, s54, 0x80
	s_add_u32 s54, s16, s44
	v_add_u32_e32 v11, s89, v11
	s_addc_u32 s55, s17, 0
	v_lshl_add_u64 v[92:93], s[54:55], 0, v[144:145]
	s_mov_b32 s44, 0
	v_mov_b32_e32 v136, 0
	v_add_u32_e32 v134, v12, v10
	v_add_u32_e32 v135, v11, v10
	v_add_u32_e32 v214, s34, v96
	v_ashrrev_i32_e32 v215, 31, v214
	v_lshlrev_b64 v[214:215], 11, v[214:215]
	v_lshl_add_u64 v[214:215], v[92:93], 0, v[214:215]
	global_load_dwordx4 v[220:223], v[214:215], off offset:1024
	v_add_u32_e32 v214, s34, v97
	v_ashrrev_i32_e32 v215, 31, v214
	v_lshlrev_b64 v[214:215], 11, v[214:215]
	v_lshl_add_u64 v[214:215], v[92:93], 0, v[214:215]
	global_load_dwordx4 v[224:227], v[214:215], off offset:1024
	v_add_u32_e32 v214, s34, v98
	v_ashrrev_i32_e32 v215, 31, v214
	v_lshlrev_b64 v[214:215], 11, v[214:215]
	v_lshl_add_u64 v[214:215], v[92:93], 0, v[214:215]
	global_load_dwordx4 v[228:231], v[214:215], off offset:1024
	v_add_u32_e32 v214, s34, v99
	v_ashrrev_i32_e32 v215, 31, v214
	v_lshlrev_b64 v[214:215], 11, v[214:215]
	v_lshl_add_u64 v[214:215], v[92:93], 0, v[214:215]
	global_load_dwordx4 v[232:235], v[214:215], off offset:1024
	v_add_u32_e32 v214, s34, v100
	v_ashrrev_i32_e32 v215, 31, v214
	v_lshlrev_b64 v[214:215], 11, v[214:215]
	v_lshl_add_u64 v[214:215], v[92:93], 0, v[214:215]
	global_load_dwordx4 v[236:239], v[214:215], off offset:1024
	v_add_u32_e32 v214, s34, v101
	v_ashrrev_i32_e32 v215, 31, v214
	v_lshlrev_b64 v[214:215], 11, v[214:215]
	v_lshl_add_u64 v[214:215], v[92:93], 0, v[214:215]
	global_load_dwordx4 v[240:243], v[214:215], off offset:1024
	v_add_u32_e32 v214, s34, v102
	v_ashrrev_i32_e32 v215, 31, v214
	v_lshlrev_b64 v[214:215], 11, v[214:215]
	v_lshl_add_u64 v[214:215], v[92:93], 0, v[214:215]
	global_load_dwordx4 v[244:247], v[214:215], off offset:1024
	v_add_u32_e32 v214, s34, v103
	v_ashrrev_i32_e32 v215, 31, v214
	v_lshlrev_b64 v[214:215], 11, v[214:215]
	v_lshl_add_u64 v[214:215], v[92:93], 0, v[214:215]
	global_load_dwordx4 v[248:251], v[214:215], off offset:1024
	v_add_u32_e32 v214, s34, v96
	v_ashrrev_i32_e32 v215, 31, v214
	v_lshlrev_b64 v[214:215], 11, v[214:215]
	v_lshl_add_u64 v[214:215], v[92:93], 0, v[214:215]
	global_load_dwordx4 v[16:19], v[214:215], off
	v_add_u32_e32 v214, s34, v97
	v_ashrrev_i32_e32 v215, 31, v214
	v_lshlrev_b64 v[214:215], 11, v[214:215]
	v_lshl_add_u64 v[214:215], v[92:93], 0, v[214:215]
	global_load_dwordx4 v[20:23], v[214:215], off
	v_add_u32_e32 v214, s34, v98
	v_ashrrev_i32_e32 v215, 31, v214
	v_lshlrev_b64 v[214:215], 11, v[214:215]
	v_lshl_add_u64 v[214:215], v[92:93], 0, v[214:215]
	global_load_dwordx4 v[24:27], v[214:215], off
	v_add_u32_e32 v214, s34, v99
	v_ashrrev_i32_e32 v215, 31, v214
	v_lshlrev_b64 v[214:215], 11, v[214:215]
	v_lshl_add_u64 v[214:215], v[92:93], 0, v[214:215]
	global_load_dwordx4 v[28:31], v[214:215], off
	v_add_u32_e32 v214, s34, v100
	v_ashrrev_i32_e32 v215, 31, v214
	v_lshlrev_b64 v[214:215], 11, v[214:215]
	v_lshl_add_u64 v[214:215], v[92:93], 0, v[214:215]
	global_load_dwordx4 v[32:35], v[214:215], off
	v_add_u32_e32 v214, s34, v101
	v_ashrrev_i32_e32 v215, 31, v214
	v_lshlrev_b64 v[214:215], 11, v[214:215]
	v_lshl_add_u64 v[214:215], v[92:93], 0, v[214:215]
	global_load_dwordx4 v[36:39], v[214:215], off
	v_add_u32_e32 v214, s34, v102
	v_ashrrev_i32_e32 v215, 31, v214
	v_lshlrev_b64 v[214:215], 11, v[214:215]
	v_lshl_add_u64 v[214:215], v[92:93], 0, v[214:215]
	global_load_dwordx4 v[40:43], v[214:215], off
	v_add_u32_e32 v214, s34, v103
	v_ashrrev_i32_e32 v215, 31, v214
	v_lshlrev_b64 v[214:215], 11, v[214:215]
	v_lshl_add_u64 v[214:215], v[92:93], 0, v[214:215]
	global_load_dwordx4 v[44:47], v[214:215], off
	s_waitcnt vmcnt(8)
	s_branch .LBB0_492

; __device__ __forceinline__ void p4_scan(const Args& a, const Frame& F) {
;     ...
;             auto prefetch = [&](int ci) {
;                 const int base = chunk_base(ci);
; #pragma unroll
;                 for (int i = 0; i < 8; ++i) { const int p = ht + 256 * i, row = p >> 4, c16 = p & 15; const int tok = base + (dir ? 127 - row : row);
;                     pq[i] = *(const u32x4*)(QKC + (size_t)tok * 1024 + h * 128 + c16 * 8); pk[i] = *(const u32x4*)(QKC + (size_t)tok * 1024 + 512 + h * 128 + c16 * 8); }
; #pragma unroll
;                 for (int i = 0; i < 2; ++i) { const int p = ht + 256 * i, row = p >> 2, cc = p & 3; const int tok = base + (dir ? 127 - row : row);
;                     pv[i] = *(const u32x4*)(PV + (size_t)tok * 512 + h * 128 + vs * 32 + cc * 8); pga[i] = GS[(size_t)hd * TA + tok]; }
; #pragma unroll
;                 for (int i = 0; i < 2; ++i) { const int idx = ht + 256 * i; if (idx < 384) { const int row = idx & 127, arr = idx >> 7; const int tok = base + (dir ? 127 - row : row); pgl[i] = GS[(size_t)(arr * 8 + hd) * TA + tok]; } }
.LBB0_492:
	s_waitcnt vmcnt(16)
	s_add_i32 s35, s44, 1
	s_cmpk_eq_i32 s44, 0x41
	s_cselect_b32 s56, s44, s35
	s_sub_i32 s58, 0x41, s56
	v_sub_co_u32_e64 v8, s[54:55], s56, 2
	s_and_b64 s[56:57], s[4:5], exec
	v_readfirstlane_b32 s56, v8
	s_cselect_b32 s56, s56, s58
	s_lshl_b32 s56, s56, 7
	s_add_i32 s56, s56, s33
	s_and_b64 s[54:55], s[54:55], exec
	s_cselect_b32 s56, s34, s56
	v_add_u32_e32 v8, s56, v104
	v_ashrrev_i32_e32 v9, 31, v8
	v_lshlrev_b64 v[10:11], 10, v[8:9]
	v_lshl_add_u64 v[10:11], v[86:87], 0, v[10:11]
	v_lshl_add_u64 v[8:9], v[8:9], 2, s[50:51]
	global_load_dwordx4 v[12:15], v[10:11], off
	global_load_dword v172, v[8:9], off
	v_add_u32_e32 v8, s56, v105
	v_ashrrev_i32_e32 v9, 31, v8
	v_lshlrev_b64 v[10:11], 10, v[8:9]
	v_lshl_add_u64 v[10:11], v[86:87], 0, v[10:11]
	v_lshl_add_u64 v[94:95], v[8:9], 2, s[50:51]
	global_load_dwordx4 v[8:11], v[10:11], off
	s_nop 0
	global_load_dword v171, v[94:95], off
	v_or_b32_e32 v94, s56, v106
	v_ashrrev_i32_e32 v95, 31, v94
	s_and_saveexec_b64 s[54:55], s[6:7]
	s_cbranch_execz .LBB0_494
	v_lshl_add_u64 v[190:191], v[94:95], 2, v[88:89]
	global_load_dword v108, v[190:191], off

; #define LAS __attribute__((address_space(3)))
; __device__ __forceinline__ unsigned cvt_pk_bf16(float lo, float hi) { unsigned r; asm volatile("v_cvt_pk_bf16_f32 %0, %1, %2" : "=v"(r) : "v"(lo), "v"(hi)); return r; }
; __device__ __forceinline__ void p4_scan(const Args& a, const Frame& F) {
;     ...
;             auto commitK = [&](int kbuf) {
; #pragma unroll
;                 for (int i = 0; i < 8; ++i) { const int p = ht + 256 * i, row = p >> 4, c16 = p & 15; *(LAS u32x4*)(L + kbuf + row * SP + c16 * 16) = pk[i]; } };
;     ...
;             auto conv_store = [&]() {
;                 const bool hi = lane >= 32;
;                 u32x4 o[4];
; #pragma unroll
;                 for (int i = 0; i < 16; ++i) { const float snd = hi ? cv[i] : cv[16 + i]; const float rcv = __shfl_xor(snd, 32);
;                     const unsigned pkd = pg8::cvt_pk_bf16(hi ? rcv : cv[i], hi ? cv[16 + i] : rcv);
;                     if ((i & 3) == 0) o[i >> 2].x = pkd; else if ((i & 3) == 1) o[i >> 2].y = pkd; else if ((i & 3) == 2) o[i >> 2].z = pkd; else o[i >> 2].w = pkd; }
;                 u32x4* dst = (u32x4*)(cD + (size_t)crow * 1024 + ck0 + (hi ? 32 : 0));
; #pragma unroll
;                 for (int j2 = 0; j2 < 4; ++j2) dst[j2] = o[j2];
;             };
.LBB0_496:
	s_or_b64 exec, exec, s[54:55]
	s_ashr_i32 s54, s56, 7
	s_add_i32 s54, s54, s76
	s_lshl_b32 s54, s54, 1
	s_ashr_i32 s55, s54, 31
	s_lshl_b64 s[54:55], s[54:55], 2
	s_add_u32 s54, s60, s54
	s_addc_u32 s55, s61, s55
	global_load_dwordx2 v[94:95], v145, s[54:55]
	s_bitcmp0_b32 s44, 0
	s_cselect_b64 s[54:55], -1, 0
	s_and_b64 s[56:57], s[54:55], exec
	s_cselect_b32 s56, 0x11000, s91
	s_add_i32 s56, s56, 0
	v_add3_u32 v144, s56, v109, v117
	ds_write_b128 v144, v[220:223]
	v_add3_u32 v48, s56, v110, v117
	ds_write_b128 v48, v[224:227]
	v_add3_u32 v48, s56, v111, v117
	ds_write_b128 v48, v[228:231]
	v_add3_u32 v48, s56, v112, v117
	ds_write_b128 v48, v[232:235]
	v_add3_u32 v48, s56, v113, v117
	ds_write_b128 v48, v[236:239]
	v_add3_u32 v48, s56, v114, v117
	ds_write_b128 v48, v[240:243]
	v_add3_u32 v48, s56, v115, v117
	ds_write_b128 v48, v[244:247]
	v_add3_u32 v48, s56, v116, v117
	ds_write_b128 v48, v[248:251]
	s_add_i32 s98, s35, 1
	s_min_i32 s98, s98, 0x41
	s_sub_i32 s99, 0x41, s98
	s_add_i32 s98, s98, -2
	s_and_b64 s[100:101], s[4:5], exec
	s_cselect_b32 s98, s98, s99
	s_lshl_b32 s98, s98, 7
	s_add_i32 s98, s98, s33
	v_add_u32_e32 v214, s98, v96
	v_ashrrev_i32_e32 v215, 31, v214
	v_lshlrev_b64 v[214:215], 11, v[214:215]
	v_lshl_add_u64 v[214:215], v[92:93], 0, v[214:215]
	global_load_dwordx4 v[220:223], v[214:215], off offset:1024
	v_add_u32_e32 v214, s98, v97
	v_ashrrev_i32_e32 v215, 31, v214
	v_lshlrev_b64 v[214:215], 11, v[214:215]
	v_lshl_add_u64 v[214:215], v[92:93], 0, v[214:215]
	global_load_dwordx4 v[224:227], v[214:215], off offset:1024
	v_add_u32_e32 v214, s98, v98
	v_ashrrev_i32_e32 v215, 31, v214
	v_lshlrev_b64 v[214:215], 11, v[214:215]
	v_lshl_add_u64 v[214:215], v[92:93], 0, v[214:215]
	global_load_dwordx4 v[228:231], v[214:215], off offset:1024
	v_add_u32_e32 v214, s98, v99
	v_ashrrev_i32_e32 v215, 31, v214
	v_lshlrev_b64 v[214:215], 11, v[214:215]
	v_lshl_add_u64 v[214:215], v[92:93], 0, v[214:215]
	global_load_dwordx4 v[232:235], v[214:215], off offset:1024
	v_add_u32_e32 v214, s98, v100
	v_ashrrev_i32_e32 v215, 31, v214
	v_lshlrev_b64 v[214:215], 11, v[214:215]
	v_lshl_add_u64 v[214:215], v[92:93], 0, v[214:215]
	global_load_dwordx4 v[236:239], v[214:215], off offset:1024
	v_add_u32_e32 v214, s98, v101
	v_ashrrev_i32_e32 v215, 31, v214
	v_lshlrev_b64 v[214:215], 11, v[214:215]
	v_lshl_add_u64 v[214:215], v[92:93], 0, v[214:215]
	global_load_dwordx4 v[240:243], v[214:215], off offset:1024
	v_add_u32_e32 v214, s98, v102
	v_ashrrev_i32_e32 v215, 31, v214
	v_lshlrev_b64 v[214:215], 11, v[214:215]
	v_lshl_add_u64 v[214:215], v[92:93], 0, v[214:215]
	global_load_dwordx4 v[244:247], v[214:215], off offset:1024
	v_add_u32_e32 v214, s98, v103
	v_ashrrev_i32_e32 v215, 31, v214
	v_lshlrev_b64 v[214:215], 11, v[214:215]
	v_lshl_add_u64 v[214:215], v[92:93], 0, v[214:215]
	global_load_dwordx4 v[248:251], v[214:215], off offset:1024
	s_waitcnt vmcnt(21)
	s_cmp_gt_u32 s44, 47
	s_cbranch_scc1 .LBB0_498
	v_cvt_pk_bf16_f32 v48, v174, v178
	v_cvt_pk_bf16_f32 v49, v182, v138
	v_cvt_pk_bf16_f32 v50, v148, v198
	v_cvt_pk_bf16_f32 v51, v202, v210
	v_cvt_pk_bf16_f32 v52, v175, v179
	v_cvt_pk_bf16_f32 v53, v183, v139
	v_cvt_pk_bf16_f32 v54, v149, v199
	v_cvt_pk_bf16_f32 v55, v203, v211
	v_cvt_pk_bf16_f32 v56, v176, v180
	v_cvt_pk_bf16_f32 v57, v184, v140
	v_cvt_pk_bf16_f32 v58, v150, v200
	v_cvt_pk_bf16_f32 v59, v204, v212
	v_cvt_pk_bf16_f32 v60, v177, v181
	v_cvt_pk_bf16_f32 v61, v185, v141
	v_cvt_pk_bf16_f32 v62, v151, v201
	v_cvt_pk_bf16_f32 v63, v205, v213
	v_add_u32_e32 v80, v80, v206
	v_ashrrev_i32_e32 v81, 31, v80
	v_lshlrev_b64 v[64:65], 11, v[80:81]
	v_lshl_add_u64 v[64:65], s[52:53], 0, v[64:65]
	v_add_u32_e32 v82, v82, v207
	v_mov_b32_e32 v83, v145
	v_lshl_add_u64 v[64:65], v[82:83], 1, v[64:65]
	s_mov_b64 s[100:101], 0x1000
	global_store_dwordx4 v[64:65], v[48:51], off
	global_store_dwordx4 v[64:65], v[52:55], off offset:2048
	s_nop 1
	v_lshl_add_u64 v[64:65], s[100:101], 0, v[64:65]
	global_store_dwordx4 v[64:65], v[56:59], off
	global_store_dwordx4 v[64:65], v[60:63], off offset:2048

; #define LAS __attribute__((address_space(3)))
; __device__ __forceinline__ float bflo(unsigned w) { return __uint_as_float(w << 16); }
; __device__ __forceinline__ void p4_scan(const Args& a, const Frame& F) {
;     ...
;             auto commitQ = [&]() {
; #pragma unroll
;                 for (int i = 0; i < 8; ++i) { const int p = ht + 256 * i, row = p >> 4, c16 = p & 15; *(LAS u32x4*)(L + S_QS + row * SP + c16 * 16) = pq[i]; } };
;             auto commitV = [&](float mprev, int vabuf) {
; #pragma unroll
;                 for (int i = 0; i < 2; ++i) { const int p = ht + 256 * i, row = p >> 2, cc = p & 3; const unsigned wv[4] = {pv[i].x, pv[i].y, pv[i].z, pv[i].w};
;                     const float av = __expf(pga[i] - fmaxf(ppx, mprev));
; #pragma unroll
;                     for (int j = 0; j < 4; ++j) { const unsigned sc2 = pg8::cvt_pk_bf16(av * bflo(wv[j]), av * bfhi(wv[j]));
;                         *(LAS bf16*)(L + S_VT + (cc * 8 + 2 * j) * SP + row * 2) = (bf16)(wv[j] & 0xffffu); *(LAS bf16*)(L + S_VT + (cc * 8 + 2 * j + 1) * SP + row * 2) = (bf16)(wv[j] >> 16);
;                         *(LAS bf16*)(L + vabuf + (cc * 8 + 2 * j) * SP + row * 2) = (bf16)(sc2 & 0xffffu); *(LAS bf16*)(L + vabuf + (cc * 8 + 2 * j + 1) * SP + row * 2) = (bf16)(sc2 >> 16); }
;                     if (cc == 0) *(LAS bf16*)(L + vabuf + 32 * SP + row * 2) = (bf16)f2bf(av); }
; #pragma unroll
;                 for (int i = 0; i < 2; ++i) { const int idx = ht + 256 * i; if (idx < 384) { const int row = idx & 127, arr = idx >> 7; *(LAS float*)(L + S_GL + arr * 512 + row * 4) = pgl[i]; } }
;             };
;             prefetch(0);
;             LDS_BARRIER();
;             commitK(S_K0); commitQ(); commitV(0.f, S_VA0);
;             float btot = pbt, pmx = ppx;
;             LDS_BARRIER();
;             const int lw = blk * 4 + (w - 4);
;             float cv[32]; bf16* cD = nullptr; int ck0 = 0, crow = 0;
;             auto conv_load = [&](int it) {
;                 const float* cW; int cN, cn;
;                 if (it < 32768) { const int e = it >> 10, sb = it & 1023; ck0 = (sb >> 6) * 64; cn = (sb & 63) * 32 + (lane & 31); cN = 2048; cW = a.in[IN_W1] + (size_t)e * 1024 * 2048; cD = (bf16*)(a.ws + WS_W1T);
;                     const int up = cn >= 1024, nn = cn & 1023; crow = e * 2048 + (nn >> 7) * 256 + up * 128 + (nn & 127); }
.LBB0_502:
	s_cmp_ge_u32 s35, 48
	s_cselect_b32 s56, 0, s56
	v_and_b32_e32 v82, 0x3c0, v48
	v_max_f32_e32 v49, v136, v136
	v_max_f32_e32 v50, v85, v85
	v_max_f32_e32 v49, v50, v49
	v_add_f32_e32 v136, v84, v49
	v_add_u32_e32 v48, v144, v206
	v_add_u32_e32 v50, v82, v207
	v_mul_u32_u24_e32 v50, s56, v50
	v_add_u32_e32 v48, v48, v50
	v_mov_b32_e32 v49, v145
	v_lshl_add_u64 v[48:49], v[48:49], 2, s[58:59]
	global_load_dwordx4 v[174:177], v[48:49], off
	v_lshl_add_u64 v[48:49], s[56:57], 2, v[48:49]
	global_load_dwordx4 v[178:181], v[48:49], off
	v_lshl_add_u64 v[48:49], s[56:57], 2, v[48:49]
	global_load_dwordx4 v[182:185], v[48:49], off
	v_lshl_add_u64 v[48:49], s[56:57], 2, v[48:49]
	global_load_dwordx4 v[138:141], v[48:49], off
	v_lshl_add_u64 v[48:49], s[56:57], 2, v[48:49]
	global_load_dwordx4 v[148:151], v[48:49], off
	v_lshl_add_u64 v[48:49], s[56:57], 2, v[48:49]
	global_load_dwordx4 v[198:201], v[48:49], off
	v_lshl_add_u64 v[48:49], s[56:57], 2, v[48:49]
	global_load_dwordx4 v[202:205], v[48:49], off
	v_lshl_add_u64 v[48:49], s[56:57], 2, v[48:49]
	global_load_dwordx4 v[210:213], v[48:49], off
	s_waitcnt lgkmcnt(0)
	s_barrier
	s_waitcnt vmcnt(16)
	ds_write_b128 v119, v[16:19]
	ds_write_b128 v120, v[20:23]
	ds_write_b128 v121, v[24:27]
	ds_write_b128 v122, v[28:31]
	ds_write_b128 v123, v[32:35]
	ds_write_b128 v124, v[36:39]
	ds_write_b128 v125, v[40:43]
	ds_write_b128 v126, v[44:47]
	v_add_u32_e32 v214, s98, v96
	v_ashrrev_i32_e32 v215, 31, v214
	v_lshlrev_b64 v[214:215], 11, v[214:215]
	v_lshl_add_u64 v[214:215], v[92:93], 0, v[214:215]
	global_load_dwordx4 v[16:19], v[214:215], off
	v_add_u32_e32 v214, s98, v97
	v_ashrrev_i32_e32 v215, 31, v214
	v_lshlrev_b64 v[214:215], 11, v[214:215]
	v_lshl_add_u64 v[214:215], v[92:93], 0, v[214:215]
	global_load_dwordx4 v[20:23], v[214:215], off
	v_add_u32_e32 v214, s98, v98
	v_ashrrev_i32_e32 v215, 31, v214
	v_lshlrev_b64 v[214:215], 11, v[214:215]
	v_lshl_add_u64 v[214:215], v[92:93], 0, v[214:215]
	global_load_dwordx4 v[24:27], v[214:215], off
	v_add_u32_e32 v214, s98, v99
	v_ashrrev_i32_e32 v215, 31, v214
	v_lshlrev_b64 v[214:215], 11, v[214:215]
	v_lshl_add_u64 v[214:215], v[92:93], 0, v[214:215]
	global_load_dwordx4 v[28:31], v[214:215], off
	v_add_u32_e32 v214, s98, v100
	v_ashrrev_i32_e32 v215, 31, v214
	v_lshlrev_b64 v[214:215], 11, v[214:215]
	v_lshl_add_u64 v[214:215], v[92:93], 0, v[214:215]
	global_load_dwordx4 v[32:35], v[214:215], off
	v_add_u32_e32 v214, s98, v101
	v_ashrrev_i32_e32 v215, 31, v214
	v_lshlrev_b64 v[214:215], 11, v[214:215]
	v_lshl_add_u64 v[214:215], v[92:93], 0, v[214:215]
	global_load_dwordx4 v[36:39], v[214:215], off
	v_add_u32_e32 v214, s98, v102
	v_ashrrev_i32_e32 v215, 31, v214
	v_lshlrev_b64 v[214:215], 11, v[214:215]
	v_lshl_add_u64 v[214:215], v[92:93], 0, v[214:215]
	global_load_dwordx4 v[40:43], v[214:215], off
	v_add_u32_e32 v214, s98, v103
	v_ashrrev_i32_e32 v215, 31, v214
	v_lshlrev_b64 v[214:215], 11, v[214:215]
	v_lshl_add_u64 v[214:215], v[92:93], 0, v[214:215]
	global_load_dwordx4 v[44:47], v[214:215], off
	v_max_f32_e32 v192, v95, v95
	v_max_f32_e32 v192, v192, v136
	v_sub_f32_e32 v193, v172, v192
	v_mul_f32_e32 v193, 0x3fb8aa3b, v193
	v_exp_f32_e32 v193, v193
	s_and_b64 s[54:55], s[54:55], exec
	v_lshlrev_b32_e32 v194, 16, v12
	v_and_b32_e32 v195, 0xffff0000, v12
	s_cselect_b32 s44, 0x1de20, s92
	v_mul_f32_e32 v194, v193, v194
	v_mul_f32_e32 v195, v193, v195
	v_cvt_pk_bf16_f32 v194, v194, v195
	v_add_u32_e32 v195, v128, v129
	s_add_i32 s44, s44, 0
	ds_write_b16 v127, v12
	ds_write_b16_d16_hi v195, v12 offset:272
	v_add_u32_e32 v12, s44, v129
	v_add_u32_e32 v196, v12, v118
	ds_write_b16 v196, v194
	ds_write_b16_d16_hi v196, v194 offset:272
	v_lshlrev_b32_e32 v194, 16, v13
	v_mul_f32_e32 v194, v193, v194
	v_and_b32_e32 v197, 0xffff0000, v13
	v_mul_f32_e32 v197, v193, v197
	v_cvt_pk_bf16_f32 v194, v194, v197
	ds_write_b16 v195, v13 offset:544
	ds_write_b16_d16_hi v195, v13 offset:816
	ds_write_b16 v196, v194 offset:544
	ds_write_b16_d16_hi v196, v194 offset:816
	v_lshlrev_b32_e32 v13, 16, v14
	v_mul_f32_e32 v13, v193, v13
	v_and_b32_e32 v194, 0xffff0000, v14
	v_mul_f32_e32 v194, v193, v194
	v_cvt_pk_bf16_f32 v13, v13, v194
	ds_write_b16 v195, v14 offset:1088
	ds_write_b16_d16_hi v195, v14 offset:1360
	ds_write_b16 v196, v13 offset:1088
	ds_write_b16_d16_hi v196, v13 offset:1360
	v_lshlrev_b32_e32 v13, 16, v15
	v_mul_f32_e32 v13, v193, v13
	v_and_b32_e32 v14, 0xffff0000, v15
	v_mul_f32_e32 v14, v193, v14
	v_cvt_pk_bf16_f32 v13, v13, v14
	ds_write_b16 v195, v15 offset:1632
	ds_write_b16_d16_hi v195, v15 offset:1904
	ds_write_b16 v196, v13 offset:1632
	ds_write_b16_d16_hi v196, v13 offset:1904
	s_and_saveexec_b64 s[54:55], s[10:11]
	v_bfe_u32 v13, v193, 16, 1
	v_add3_u32 v13, v193, v13, s93
	v_add_u32_e32 v14, s44, v118
	ds_write_b16_d16_hi v14, v13 offset:8704
	s_or_b64 exec, exec, s[54:55]
	v_sub_f32_e32 v13, v171, v192
	v_mul_f32_e32 v13, 0x3fb8aa3b, v13
	v_exp_f32_e32 v13, v13
	v_lshlrev_b32_e32 v14, 16, v8
	v_and_b32_e32 v15, 0xffff0000, v8
	v_mul_f32_e32 v14, v13, v14
	v_mul_f32_e32 v15, v13, v15
	v_cvt_pk_bf16_f32 v14, v14, v15
	ds_write_b16 v131, v8
	ds_write_b16_d16_hi v132, v8 offset:272
	v_add_u32_e32 v8, v12, v130
	v_lshlrev_b32_e32 v12, 16, v9
	ds_write_b16 v8, v14
	ds_write_b16_d16_hi v8, v14 offset:272
	v_mul_f32_e32 v12, v13, v12
	v_and_b32_e32 v14, 0xffff0000, v9
	v_mul_f32_e32 v14, v13, v14
	v_cvt_pk_bf16_f32 v12, v12, v14
	ds_write_b16 v132, v9 offset:544
	ds_write_b16_d16_hi v132, v9 offset:816
	ds_write_b16 v8, v12 offset:544
	ds_write_b16_d16_hi v8, v12 offset:816
	v_lshlrev_b32_e32 v9, 16, v10
	v_mul_f32_e32 v9, v13, v9
	v_and_b32_e32 v12, 0xffff0000, v10
	v_mul_f32_e32 v12, v13, v12
	v_cvt_pk_bf16_f32 v9, v9, v12
	ds_write_b16 v132, v10 offset:1088
	ds_write_b16_d16_hi v132, v10 offset:1360
	ds_write_b16 v8, v9 offset:1088
	ds_write_b16_d16_hi v8, v9 offset:1360
	v_lshlrev_b32_e32 v9, 16, v11
	v_mul_f32_e32 v9, v13, v9
	v_and_b32_e32 v10, 0xffff0000, v11
	v_mul_f32_e32 v10, v13, v10
	v_cvt_pk_bf16_f32 v9, v9, v10
	ds_write_b16 v132, v11 offset:1632
	ds_write_b16_d16_hi v132, v11 offset:1904
	ds_write_b16 v8, v9 offset:1632
	ds_write_b16_d16_hi v8, v9 offset:1904
	s_and_saveexec_b64 s[54:55], s[10:11]
	s_cbranch_execnz .LBB0_507
	s_or_b64 exec, exec, s[54:55]
	s_and_saveexec_b64 s[54:55], s[6:7]
	s_cbranch_execnz .LBB0_508
